# attention-A tile loop: fixed scalar bases for K/V staging DMAs with lane offsets advanced per tile (no 64-bit scalar address adds / running base), max chain starts with one v_max, dead s27 update remo
# speedup vs baseline: 1.0095x; 1.0030x over previous
.Lpro_noconv:
	s_cmp_lg_u64 s[12:13], 0
	s_cselect_b64 s[54:55], -1, 0
	s_cmp_lt_u32 s0, 2
	s_mov_b32 s0, 0x3f400000
	s_cselect_b64 s[52:53], -1, 0
	s_mov_b32 s8, s9
	v_mfma_scale_f32_32x32x64_f8f6f4 v[16:31], v[12:17], v[182:187], 0, v217, v216 op_sel_hi:[0,0,0] cbsz:2 blgp:2
	s_nop 4
	v_max_f32_e32 v52, v33, v33
	v_max_f32_e32 v53, v32, v32
	v_max_f32_e32 v52, v53, v52
	v_max3_f32 v52, v52, v34, v35
	v_max3_f32 v52, v52, v36, v37
	v_max3_f32 v52, v52, v38, v39
	v_max3_f32 v52, v52, v40, v41
	v_mfma_scale_f32_32x32x64_f8f6f4 v[16:31], v[58:63], v[176:181], v[16:31], v217, v216 op_sel_hi:[0,0,0] cbsz:2 blgp:2
	v_max3_f32 v52, v52, v42, v43
	v_max3_f32 v52, v52, v44, v45
	v_max3_f32 v52, v52, v46, v47
	s_mov_b32 s10, s9
	s_mov_b32 s11, s9
	s_mov_b32 s12, s9
	s_mov_b32 s13, s9
	s_nop 4
	v_max3_f32 v52, v52, v16, v17
	v_max3_f32 v52, v52, v18, v19
	v_max3_f32 v52, v52, v20, v21
	v_max3_f32 v52, v52, v22, v23
	v_max3_f32 v52, v52, v24, v25
	v_max3_f32 v52, v52, v26, v27
	v_max3_f32 v52, v52, v28, v29
	v_max3_f32 v52, v52, v30, v31
	v_mov_b32_e32 v53, v52
	s_nop 1
	v_permlane32_swap_b32_e32 v52, v53
	v_max_f32_e32 v53, v53, v53
	v_max_f32_e32 v52, v52, v52
	v_max_f32_e32 v52, v52, v53
	v_add_f32_e32 v53, 0x7149f2ca, v52
	v_cmp_ge_f32_e32 vcc, s0, v53
	v_max_f32_e32 v52, 0xf149f2ca, v52
	s_cmp_lg_u64 vcc, exec
	v_add_f32_e32 v52, 2.0, v52
	s_cselect_b64 vcc, -1, 0
	v_cndmask_b32_e32 v52, v219, v52, vcc
	v_add_f32_e32 v53, -4.0, v52
	s_lshl_b32 s0, s46, 2
	v_sub_f32_e32 v32, v32, v53
	v_sub_f32_e32 v33, v33, v53
	v_sub_f32_e32 v34, v34, v53
	v_sub_f32_e32 v35, v35, v53
	v_sub_f32_e32 v36, v36, v53
	v_sub_f32_e32 v37, v37, v53
	v_sub_f32_e32 v38, v38, v53
	v_sub_f32_e32 v39, v39, v53
	v_sub_f32_e32 v40, v40, v53
	v_sub_f32_e32 v41, v41, v53
	v_sub_f32_e32 v42, v42, v53
	v_sub_f32_e32 v43, v43, v53
	v_sub_f32_e32 v44, v44, v53
	v_sub_f32_e32 v45, v45, v53
	v_sub_f32_e32 v46, v46, v53
	v_sub_f32_e32 v47, v47, v53
	s_add_i32 s0, s0, 0
	s_mov_b32 s14, s9
	s_mov_b32 s15, s9
	s_mov_b32 s16, s9
	s_mov_b32 s17, s9
	s_mov_b32 s18, s9
	s_mov_b32 s19, s9
	s_mov_b32 s20, s9
	s_mov_b32 s21, s9
	s_mov_b32 s22, s9
	s_mov_b32 s23, s9
	v_mov_b64_e32 v[0:1], s[8:9]
	v_exp_f32_e32 v144, v32
	v_exp_f32_e32 v145, v33
	v_exp_f32_e32 v146, v34
	v_exp_f32_e32 v147, v35
	v_exp_f32_e32 v148, v36
	v_exp_f32_e32 v149, v37
	v_exp_f32_e32 v150, v38
	v_exp_f32_e32 v151, v39
	v_exp_f32_e32 v152, v40
	v_exp_f32_e32 v153, v41
	v_exp_f32_e32 v154, v42
	v_exp_f32_e32 v155, v43
	v_exp_f32_e32 v156, v44
	v_exp_f32_e32 v157, v45
	v_exp_f32_e32 v158, v46
	v_exp_f32_e32 v159, v47
	s_add_i32 s0, s0, 0x1c800
	v_mov_b64_e32 v[2:3], s[10:11]
	v_mov_b64_e32 v[4:5], s[12:13]
	v_mov_b64_e32 v[6:7], s[14:15]
	v_mov_b64_e32 v[8:9], s[16:17]
	v_mov_b64_e32 v[10:11], s[18:19]
	v_mov_b64_e32 v[12:13], s[20:21]
	v_mov_b64_e32 v[14:15], s[22:23]
	v_sub_f32_e32 v128, v16, v53
	s_and_b64 s[10:11], s[52:53], exec
	v_lshlrev_b32_e32 v16, 7, v48
	v_sub_f32_e32 v80, 4.0, v52
	v_sub_f32_e32 v143, v31, v53
	v_sub_f32_e32 v142, v30, v53
	v_sub_f32_e32 v141, v29, v53
	v_sub_f32_e32 v140, v28, v53
	v_sub_f32_e32 v139, v27, v53
	v_sub_f32_e32 v138, v26, v53
	v_sub_f32_e32 v137, v25, v53
	v_sub_f32_e32 v136, v24, v53
	v_sub_f32_e32 v135, v23, v53
	v_sub_f32_e32 v134, v22, v53
	v_sub_f32_e32 v133, v21, v53
	v_sub_f32_e32 v132, v20, v53
	v_sub_f32_e32 v131, v19, v53
	v_sub_f32_e32 v130, v18, v53
	v_sub_f32_e32 v129, v17, v53
	s_cselect_b32 s14, 23, 22
	v_add3_u32 v164, s85, v16, v51
	s_add_u32 s10, s78, s4
	v_add_u32_e32 v174, v49, v50
	v_mov_b64_e32 v[62:63], v[14:15]
	v_mov_b64_e32 v[46:47], v[14:15]
	v_mov_b64_e32 v[30:31], v[14:15]
	v_mov_b64_e32 v[78:79], v[14:15]
	s_mov_b32 s1, 2
	s_mov_b32 s57, 1
	s_mov_b32 s27, -2
	v_mov_b32_e32 v81, v80
	v_mov_b32_e32 v82, v80
	v_mov_b32_e32 v83, v80
	v_mov_b32_e32 v84, v80
	v_mov_b32_e32 v85, v80
	v_mov_b32_e32 v86, v80
	v_mov_b32_e32 v87, v80
	v_mov_b32_e32 v88, v80
	v_mov_b32_e32 v89, v80
	v_mov_b32_e32 v90, v80
	v_mov_b32_e32 v91, v80
	v_mov_b32_e32 v92, v80
	v_mov_b32_e32 v93, v80
	v_mov_b32_e32 v94, v80
	v_mov_b32_e32 v95, v80
	s_mov_b32 s15, 0
	v_mov_b32_e32 v165, v167
	s_addc_u32 s11, s79, s5
	v_mov_b32_e32 v175, v167
	v_mov_b64_e32 v[60:61], v[12:13]
	v_mov_b64_e32 v[58:59], v[10:11]
	v_mov_b64_e32 v[56:57], v[8:9]
	v_mov_b64_e32 v[54:55], v[6:7]
	v_mov_b64_e32 v[52:53], v[4:5]
	v_mov_b64_e32 v[50:51], v[2:3]
	v_mov_b64_e32 v[48:49], v[0:1]
	v_mov_b64_e32 v[44:45], v[12:13]
	v_mov_b64_e32 v[42:43], v[10:11]
	v_mov_b64_e32 v[40:41], v[8:9]
	v_mov_b64_e32 v[38:39], v[6:7]
	v_mov_b64_e32 v[36:37], v[4:5]
	v_mov_b64_e32 v[34:35], v[2:3]
	v_mov_b64_e32 v[32:33], v[0:1]
	v_mov_b64_e32 v[28:29], v[12:13]
	v_mov_b64_e32 v[26:27], v[10:11]
	v_mov_b64_e32 v[24:25], v[8:9]
	v_mov_b64_e32 v[22:23], v[6:7]
	v_mov_b64_e32 v[20:21], v[4:5]
	v_mov_b64_e32 v[18:19], v[2:3]
	v_mov_b64_e32 v[16:17], v[0:1]
	s_mov_b32 s16, 2
	v_mov_b64_e32 v[76:77], v[12:13]
	v_mov_b64_e32 v[74:75], v[10:11]
	v_mov_b64_e32 v[72:73], v[8:9]
	v_mov_b64_e32 v[70:71], v[6:7]
	v_mov_b64_e32 v[68:69], v[4:5]
	v_mov_b64_e32 v[66:67], v[2:3]
	v_mov_b64_e32 v[64:65], v[0:1]
	v_mbcnt_lo_u32_b32 v200, -1, 0
	v_mbcnt_hi_u32_b32 v200, -1, v200
	v_lshrrev_b32_e32 v201, 3, v200
	v_mul_lo_u32 v201, v201, s56
	v_lshlrev_b32_e32 v200, 4, v200
	v_and_b32_e32 v200, 0x70, v200
	v_lshl_or_b32 v214, v201, 2, v200
	v_mov_b32_e32 v215, v214
	s_mov_b64 s[98:99], s[58:59]
	s_add_i32 s100, s66, 0xc800
	s_lshl_b32 s101, s56, 5
	s_movk_i32 s15, 0x70
	ds_read_b128 v[228:231], v223 offset:8192
	ds_read_b64 v[232:233], v224 offset:8192
	ds_read_b128 v[234:237], v223 offset:12288
	ds_read_b64 v[238:239], v224 offset:12288
	ds_read_b128 v[240:243], v221 offset:8192
	ds_read_b64 v[244:245], v222 offset:8192
	ds_read_b128 v[246:249], v221 offset:12288
	ds_read_b64 v[250:251], v222 offset:12288
	v_mbcnt_lo_u32_b32 v200, -1, 0
	v_mbcnt_hi_u32_b32 v200, -1, v200
	v_and_b32_e32 v201, 7, v200
	v_ashrrev_i32_e32 v202, 3, v200
	v_lshlrev_b32_e32 v203, 2, v200
	v_lshl_add_u32 v204, v201, 10, s66
	v_lshlrev_b32_e32 v205, 2, v202
	v_and_b32_e32 v205, 12, v205
	v_add_u32_e32 v204, 0xc800, v204
	v_add_u32_e32 v204, v204, v205
	v_add_u32_e32 v206, v202, v203
	v_add_u32_e32 v207, 8, v206
	v_add_u32_e32 v208, 16, v206
	v_add_u32_e32 v209, 24, v206
	v_and_b32_e32 v206, 28, v206
	v_and_b32_e32 v207, 28, v207
	v_and_b32_e32 v208, 28, v208
	v_and_b32_e32 v209, 28, v209
	v_lshl_add_u32 v206, v206, 2, v204
	v_lshl_add_u32 v207, v207, 2, v204
	v_lshl_add_u32 v208, v208, 2, v204
	v_lshl_add_u32 v209, v209, 2, v204
	v_mul_u32_u24_e32 v210, s48, v202
	v_lshl_add_u32 v210, v201, 3, v210
	v_lshl_add_u32 v211, v201, 5, s0
	v_lshl_add_u32 v205, v200, 4, s89
	ds_write_b128 v205, v[206:209] offset:16384
	ds_write_b64 v205, v[210:211] offset:40960
	s_add_u32 s16, s10, 0x74802000
	s_addc_u32 s17, s11, 0
	s_add_u32 s10, s10, 0x74006000
	s_addc_u32 s11, s11, 0

.LBB0_417:
	s_add_i32 m0, s89, 0x2000
	s_barrier
	global_load_lds_dwordx4 v164, s[10:11]
	v_add_u32_e32 v164, 0x2000, v164
	s_add_i32 m0, s89, 0x8000
	s_andn2_b64 vcc, exec, s[62:63]
	global_load_lds_dwordx4 v174, s[16:17]
	v_add_u32_e32 v174, 0x2000, v174
	s_cbranch_vccnz .LBB0_419
	s_add_u32 s98, s98, s101
	s_addc_u32 s99, s99, 0
	s_add_i32 s100, s100, 0x400
	s_mov_b32 m0, s100
	v_add_u32_e32 v96, -16, v215
	v_bfi_b32 v215, s15, v96, v215
	global_load_lds_dwordx4 v215, s[98:99] nt
.LBB0_419:
	v_mfma_scale_f32_32x32x64_f8f6f4 v[112:127], v[228:233], v[182:187], v[80:95], v217, v216 op_sel_hi:[0,0,0] cbsz:2 blgp:2
	v_exp_f32_e32 v128, v128
	v_exp_f32_e32 v129, v129
	v_exp_f32_e32 v130, v130
	v_exp_f32_e32 v131, v131
	v_mfma_scale_f32_32x32x64_f8f6f4 v[96:111], v[234:239], v[182:187], v[80:95], v217, v216 op_sel_hi:[0,0,0] cbsz:2 blgp:2
	v_exp_f32_e32 v132, v132
	v_exp_f32_e32 v133, v133
	v_exp_f32_e32 v134, v134
	v_exp_f32_e32 v135, v135
	v_mfma_scale_f32_32x32x64_f8f6f4 v[112:127], v[240:245], v[176:181], v[112:127], v217, v216 op_sel_hi:[0,0,0] cbsz:2 blgp:2
	v_exp_f32_e32 v136, v136
	v_exp_f32_e32 v137, v137
	v_exp_f32_e32 v138, v138
	v_exp_f32_e32 v139, v139
	v_mfma_scale_f32_32x32x64_f8f6f4 v[96:111], v[246:251], v[176:181], v[96:111], v217, v216 op_sel_hi:[0,0,0] cbsz:2 blgp:2
	ds_read_b128 v[228:231], v223
	ds_read_b64 v[232:233], v224
	ds_read_b128 v[234:237], v223 offset:4096
	ds_read_b64 v[238:239], v224 offset:4096
	ds_read_b128 v[240:243], v221
	ds_read_b64 v[244:245], v222
	ds_read_b128 v[246:249], v221 offset:4096
	ds_read_b64 v[250:251], v222 offset:4096
	ds_read_b128 v[206:209], v163 offset:24576
	ds_read_b64 v[210:211], v220 offset:24576
	ds_read_b128 v[200:203], v163 offset:26624
	ds_read_b64 v[204:205], v220 offset:26624
	ds_read_b128 v[194:197], v163 offset:28672
	ds_read_b64 v[198:199], v220 offset:28672
	ds_read_b128 v[188:191], v163 offset:30720
	ds_read_b64 v[192:193], v220 offset:30720
	v_exp_f32_e32 v140, v140
	v_exp_f32_e32 v141, v141
	v_exp_f32_e32 v142, v142
	v_exp_f32_e32 v143, v143
	v_max_f32_e32 v225, v112, v113
	v_cvt_scalef32_2xpk16_bf6_f32 v[128:133], v[144:159], v[128:143], 1.0
	v_max3_f32 v225, v225, v114, v115
	v_max3_f32 v225, v225, v116, v117
	v_mfma_scale_f32_32x32x64_f8f6f4 v[64:79], v[128:133], v[168:173], v[64:79], v218, v218 op_sel_hi:[0,0,0] cbsz:3 blgp:2
	s_waitcnt lgkmcnt(0)
	v_mfma_scale_f32_32x32x64_f8f6f4 v[0:15], v[128:133], v[206:211], v[0:15], v218, v217 op_sel_hi:[0,0,0] cbsz:3 blgp:2
	v_max3_f32 v225, v225, v118, v119
	v_max3_f32 v225, v225, v120, v121
	v_max3_f32 v225, v225, v122, v123
	v_mfma_scale_f32_32x32x64_f8f6f4 v[48:63], v[128:133], v[200:205], v[48:63], v218, v217 op_sel_hi:[0,0,0] cbsz:3 blgp:2
	v_max3_f32 v225, v225, v124, v125
	v_max3_f32 v225, v225, v126, v127
	v_max3_f32 v225, v225, v96, v97
	v_max3_f32 v225, v225, v98, v99
	v_mfma_scale_f32_32x32x64_f8f6f4 v[32:47], v[128:133], v[194:199], v[32:47], v218, v217 op_sel_hi:[0,0,0] cbsz:3 blgp:2
	v_max3_f32 v225, v225, v100, v101
	v_max3_f32 v225, v225, v102, v103
	v_max3_f32 v225, v225, v104, v105
	v_max3_f32 v225, v225, v106, v107
	v_mfma_scale_f32_32x32x64_f8f6f4 v[16:31], v[128:133], v[188:193], v[16:31], v218, v217 op_sel_hi:[0,0,0] cbsz:3 blgp:2
	v_max3_f32 v225, v225, v108, v109
	v_max3_f32 v225, v225, v110, v111
	v_cmp_nge_f32_e32 vcc, s2, v225
	s_cbranch_vccnz .LBB0_444

.LBB0_428:
	s_mov_b32 m0, s89
	s_barrier
	global_load_lds_dwordx4 v164, s[10:11]
	v_add_u32_e32 v164, 0x2000, v164
	s_add_i32 m0, s89, 0x6000
	s_and_b64 vcc, exec, s[60:61]
	global_load_lds_dwordx4 v174, s[16:17]
	v_add_u32_e32 v174, 0x2000, v174
	s_cbranch_vccnz .LBB0_437
	s_bfe_u32 s4, s1, 0x30000
	s_cbranch_scc0 .LBB0_432
	s_add_u32 s98, s98, s101
	s_addc_u32 s99, s99, 0
	s_add_i32 s100, s100, 0x400
	s_mov_b32 m0, s100
	v_add_u32_e32 v128, -16, v215
	v_bfi_b32 v215, s15, v128, v215
	global_load_lds_dwordx4 v215, s[98:99] nt
.LBB0_437:
	v_mfma_scale_f32_32x32x64_f8f6f4 v[144:159], v[228:233], v[182:187], v[80:95], v217, v216 op_sel_hi:[0,0,0] cbsz:2 blgp:2
	v_exp_f32_e32 v96, v96
	v_exp_f32_e32 v97, v97
	v_exp_f32_e32 v98, v98
	v_exp_f32_e32 v99, v99
	v_mfma_scale_f32_32x32x64_f8f6f4 v[128:143], v[234:239], v[182:187], v[80:95], v217, v216 op_sel_hi:[0,0,0] cbsz:2 blgp:2
	v_exp_f32_e32 v100, v100
	v_exp_f32_e32 v101, v101
	v_exp_f32_e32 v102, v102
	v_exp_f32_e32 v103, v103
	v_mfma_scale_f32_32x32x64_f8f6f4 v[144:159], v[240:245], v[176:181], v[144:159], v217, v216 op_sel_hi:[0,0,0] cbsz:2 blgp:2
	v_exp_f32_e32 v104, v104
	v_exp_f32_e32 v105, v105
	v_exp_f32_e32 v106, v106
	v_exp_f32_e32 v107, v107
	v_mfma_scale_f32_32x32x64_f8f6f4 v[128:143], v[246:251], v[176:181], v[128:143], v217, v216 op_sel_hi:[0,0,0] cbsz:2 blgp:2
	ds_read_b128 v[228:231], v223 offset:8192
	ds_read_b64 v[232:233], v224 offset:8192
	ds_read_b128 v[234:237], v223 offset:12288
	ds_read_b64 v[238:239], v224 offset:12288
	ds_read_b128 v[240:243], v221 offset:8192
	ds_read_b64 v[244:245], v222 offset:8192
	ds_read_b128 v[246:249], v221 offset:12288
	ds_read_b64 v[250:251], v222 offset:12288
	ds_read_b128 v[206:209], v163 offset:32768
	ds_read_b64 v[210:211], v220 offset:32768
	ds_read_b128 v[200:203], v163 offset:34816
	ds_read_b64 v[204:205], v220 offset:34816
	ds_read_b128 v[194:197], v163 offset:36864
	ds_read_b64 v[198:199], v220 offset:36864
	ds_read_b128 v[188:191], v163 offset:38912
	ds_read_b64 v[192:193], v220 offset:38912
	v_exp_f32_e32 v108, v108
	v_exp_f32_e32 v109, v109
	v_exp_f32_e32 v110, v110
	v_exp_f32_e32 v111, v111
	v_max_f32_e32 v212, v144, v145
	v_cvt_scalef32_2xpk16_bf6_f32 v[96:101], v[112:127], v[96:111], 1.0
	v_max3_f32 v212, v212, v146, v147
	v_max3_f32 v212, v212, v148, v149
	v_mfma_scale_f32_32x32x64_f8f6f4 v[64:79], v[96:101], v[168:173], v[64:79], v218, v218 op_sel_hi:[0,0,0] cbsz:3 blgp:2
	s_waitcnt lgkmcnt(0)
	v_mfma_scale_f32_32x32x64_f8f6f4 v[0:15], v[96:101], v[206:211], v[0:15], v218, v217 op_sel_hi:[0,0,0] cbsz:3 blgp:2
	v_max3_f32 v212, v212, v150, v151
	v_max3_f32 v212, v212, v152, v153
	v_max3_f32 v212, v212, v154, v155
	v_mfma_scale_f32_32x32x64_f8f6f4 v[48:63], v[96:101], v[200:205], v[48:63], v218, v217 op_sel_hi:[0,0,0] cbsz:3 blgp:2
	v_max3_f32 v212, v212, v156, v157
	v_max3_f32 v212, v212, v158, v159
	v_max3_f32 v212, v212, v128, v129
	v_max3_f32 v212, v212, v130, v131
	v_mfma_scale_f32_32x32x64_f8f6f4 v[32:47], v[96:101], v[194:199], v[32:47], v218, v217 op_sel_hi:[0,0,0] cbsz:3 blgp:2
	v_max3_f32 v212, v212, v132, v133
	v_max3_f32 v212, v212, v134, v135
	v_max3_f32 v212, v212, v136, v137
	v_max3_f32 v212, v212, v138, v139
	v_mfma_scale_f32_32x32x64_f8f6f4 v[16:31], v[96:101], v[188:193], v[16:31], v218, v217 op_sel_hi:[0,0,0] cbsz:3 blgp:2
	v_max3_f32 v212, v212, v140, v141
	v_max3_f32 v212, v212, v142, v143
	v_cmp_nge_f32_e32 vcc, s2, v212
	s_cbranch_vccnz .LBB0_445
.LBB0_442:
	v_exp_f32_e32 v144, v144
	v_exp_f32_e32 v145, v145
	v_exp_f32_e32 v146, v146
	v_exp_f32_e32 v147, v147
	v_exp_f32_e32 v148, v148
	v_exp_f32_e32 v149, v149
	v_exp_f32_e32 v150, v150
	v_exp_f32_e32 v151, v151
	v_exp_f32_e32 v152, v152
	v_exp_f32_e32 v153, v153
	v_exp_f32_e32 v154, v154
	v_exp_f32_e32 v155, v155
	v_exp_f32_e32 v156, v156
	v_exp_f32_e32 v157, v157
	v_exp_f32_e32 v158, v158
	v_exp_f32_e32 v159, v159
	s_add_i32 s1, s1, 2
	s_cmpk_gt_u32 s1, 0xff
	s_cbranch_scc0 .Lattn_top
	s_branch .LBB0_446

.LBB0_450:
	s_barrier
	s_add_i32 m0, s89, 0x8000
	s_nop 0
	global_load_lds_dwordx4 v174, s[16:17]
	s_and_b64 vcc, exec, s[60:61]
	s_cbranch_vccnz .LBB0_452
	v_mbcnt_lo_u32_b32 v98, -1, 0
	v_mbcnt_hi_u32_b32 v98, -1, v98
	s_mov_b32 m0, s88
	v_ashrrev_i32_e32 v96, 3, v98
	v_add_u32_e32 v96, 56, v96
	v_lshl_add_u32 v98, v98, 2, 4
	v_mad_i64_i32 v[96:97], s[10:11], s56, v96, 0
	v_and_b32_e32 v98, 28, v98
	v_lshl_add_u64 v[96:97], v[96:97], 2, s[58:59]
	v_lshlrev_b32_e32 v166, 2, v98
	v_lshl_add_u64 v[96:97], v[96:97], 0, v[166:167]
	s_mov_b64 s[10:11], 0x1f000000
	v_lshl_add_u64 v[96:97], v[96:97], 0, s[10:11]
	global_load_lds_dwordx4 v[96:97], off nt
